# FoX: static s_setprio 1 for waves 4-7 during the forgetting-attention items (reset before the XCD barrier)
# speedup vs baseline: 1.0271x; 1.0021x over previous
.LBB0_1794:
	v_readlane_b32 s1, v253, 30
	s_cmp_lt_u32 s1, 4
	s_cbranch_scc1 .Lfox_prio_done
	s_setprio 1

.LBB0_1891:
	v_readlane_b32 s84, v253, 22
	s_setprio 0
	v_readlane_b32 s52, v253, 31
	v_readlane_b32 s86, v253, 24
	v_readlane_b32 s87, v253, 25
	v_readlane_b32 s88, v253, 26
	v_readlane_b32 s89, v253, 27
	v_readlane_b32 s90, v253, 28
	v_readlane_b32 s91, v253, 29
	v_readlane_b32 s96, v253, 61
	v_readlane_b32 s97, v252, 3
	v_readlane_b32 s94, v253, 30
	v_readlane_b32 s53, v253, 32
	v_readlane_b32 s56, v253, 35
	v_readlane_b32 s57, v253, 36
	v_readlane_b32 s92, v253, 47
	v_readlane_b32 s70, v252, 0
	v_readlane_b32 s85, v253, 23
	v_readlane_b32 s54, v253, 33
	v_readlane_b32 s55, v253, 34
	v_readlane_b32 s58, v253, 37
	v_readlane_b32 s59, v253, 38
	v_readlane_b32 s60, v253, 39
	v_readlane_b32 s61, v253, 40
	v_readlane_b32 s62, v253, 41
	v_readlane_b32 s63, v253, 42
	v_readlane_b32 s64, v253, 43
	v_readlane_b32 s65, v253, 44
	v_readlane_b32 s66, v253, 45
	v_readlane_b32 s67, v253, 46
